# LRU pass 1: the 64-token scan's sixteen LDS reads issued together (counted waits) instead of one round trip per step; on top of router loop rewrite
# speedup vs baseline: 1.0034x; 1.0034x over previous
; #define LAS __attribute__((address_space(3)))
; __device__ __forceinline__ float sigmoidf_(float x) { return __builtin_amdgcn_rcpf(1.0f + __expf(-x)); }
; template <int PASS>
; __device__ __forceinline__ void lru_phase(const Args& a, Frame& F, int l) {
;     ...
;             __syncthreads();
;             f32x4 acc[4][2];
; #pragma unroll
;             for (int m = 0; m < 4; ++m) { acc[m][0] = (f32x4){0.f, 0.f, 0.f, 0.f}; acc[m][1] = (f32x4){0.f, 0.f, 0.f, 0.f}; }
; #pragma unroll
;             for (int ks = 0; ks < 4; ++ks)
; #pragma unroll
;                 for (int m = 0; m < 4; ++m) { const bf16x8 Af = *(const LAS bf16x8*)(XA + (16 * m + fr) * 136 + 32 * ks + 8 * fq);
;                     acc[m][0] = __builtin_amdgcn_mfma_f32_16x16x32_bf16(Af, Bf[0][ks], acc[m][0], 0, 0, 0);
;                     acc[m][1] = __builtin_amdgcn_mfma_f32_16x16x32_bf16(Af, Bf[1][ks], acc[m][1], 0, 0, 0); }
;             { const int j = 16 * w + fr; const float bav = bav_u, bxv = bxv_u, sp = sp_u;
; #pragma unroll
;                 for (int m = 0; m < 4; ++m)
; #pragma unroll
;                     for (int r = 0; r < 4; ++r) { const int tt = 16 * m + 4 * fq + r;
;                         const float rr = sigmoidf_(acc[m][0][r] + bav), ii = sigmoidf_(acc[m][1][r] + bxv);
;                         const float la = -8.0f * rr * sp; const float av = __expf(la); const float mult = __builtin_amdgcn_sqrtf(neg_expm1f(2.0f * la));
;                         const float xcv = XC[tt * 128 + j]; (void)av; AA[tt * 128 + j] = (float)(_Float16)la; XC[tt * 128 + j] = (float)(_Float16)(mult * ii * xcv); } }
.LBB0_357:
	s_waitcnt lgkmcnt(0)
	s_barrier
	ds_read_b128 v[68:71], v125
	ds_read_b128 v[130:133], v125 offset:64
	ds_read_b128 v[76:79], v125 offset:4352
	ds_read_b128 v[84:87], v125 offset:8704
	ds_read_b128 v[92:95], v125 offset:13056
	s_add_i32 s0, s2, s12
	s_waitcnt lgkmcnt(4)
	v_mfma_f32_16x16x32_bf16 v[72:75], v[68:71], v[4:7], 0
	s_lshl_b32 s3, s0, 6
	v_and_b32_e32 v0, 0x7f, v128
	v_ashrrev_i32_e32 v2, 7, v128
	v_mfma_f32_16x16x32_bf16 v[68:71], v[68:71], v[20:23], 0
	s_waitcnt lgkmcnt(3)
	v_mfma_f32_16x16x32_bf16 v[72:75], v[130:133], v[8:11], v[72:75]
	v_mfma_f32_16x16x32_bf16 v[68:71], v[130:133], v[24:27], v[68:71]
	ds_read_b128 v[130:133], v125 offset:4416
	s_waitcnt lgkmcnt(3)
	v_mfma_f32_16x16x32_bf16 v[80:83], v[76:79], v[4:7], 0
	v_mfma_f32_16x16x32_bf16 v[76:79], v[76:79], v[20:23], 0
	s_waitcnt lgkmcnt(0)
	v_mfma_f32_16x16x32_bf16 v[80:83], v[130:133], v[8:11], v[80:83]
	v_mfma_f32_16x16x32_bf16 v[76:79], v[130:133], v[24:27], v[76:79]
	ds_read_b128 v[130:133], v125 offset:8768
	v_mfma_f32_16x16x32_bf16 v[88:91], v[84:87], v[4:7], 0
	v_mfma_f32_16x16x32_bf16 v[84:87], v[84:87], v[20:23], 0
	s_waitcnt lgkmcnt(0)
	v_mfma_f32_16x16x32_bf16 v[88:91], v[130:133], v[8:11], v[88:91]
	v_mfma_f32_16x16x32_bf16 v[84:87], v[130:133], v[24:27], v[84:87]
	ds_read_b128 v[130:133], v125 offset:13120
	v_mfma_f32_16x16x32_bf16 v[96:99], v[92:95], v[4:7], 0
	v_mfma_f32_16x16x32_bf16 v[92:95], v[92:95], v[20:23], 0
	s_waitcnt lgkmcnt(0)
	v_mfma_f32_16x16x32_bf16 v[96:99], v[130:133], v[8:11], v[96:99]
	v_mfma_f32_16x16x32_bf16 v[92:95], v[130:133], v[24:27], v[92:95]
	ds_read_b128 v[130:133], v125 offset:128
	s_waitcnt lgkmcnt(0)
	v_mfma_f32_16x16x32_bf16 v[72:75], v[130:133], v[12:15], v[72:75]
	v_mfma_f32_16x16x32_bf16 v[68:71], v[130:133], v[28:31], v[68:71]
	ds_read_b128 v[130:133], v125 offset:4480
	s_waitcnt lgkmcnt(0)
	v_mfma_f32_16x16x32_bf16 v[80:83], v[130:133], v[12:15], v[80:83]
	v_mfma_f32_16x16x32_bf16 v[76:79], v[130:133], v[28:31], v[76:79]
	ds_read_b128 v[130:133], v125 offset:8832
	s_waitcnt lgkmcnt(0)
	v_mfma_f32_16x16x32_bf16 v[134:137], v[130:133], v[12:15], v[88:91]
	v_mfma_f32_16x16x32_bf16 v[130:133], v[130:133], v[28:31], v[84:87]
	s_nop 2
	ds_read_b128 v[84:87], v125 offset:13184
	s_waitcnt lgkmcnt(0)
	v_mfma_f32_16x16x32_bf16 v[138:141], v[84:87], v[12:15], v[96:99]
	v_mfma_f32_16x16x32_bf16 v[142:145], v[84:87], v[28:31], v[92:95]
	ds_read_b128 v[84:87], v125 offset:192
	s_waitcnt lgkmcnt(0)
	v_mfma_f32_16x16x32_bf16 v[92:95], v[84:87], v[32:35], v[68:71]
	s_nop 2
	ds_read_b128 v[68:71], v125 offset:4544
	v_mfma_f32_16x16x32_bf16 v[96:99], v[84:87], v[16:19], v[72:75]
	s_waitcnt lgkmcnt(0)
	v_mfma_f32_16x16x32_bf16 v[88:91], v[68:71], v[16:19], v[80:83]
	s_nop 5
	v_add_f32_e32 v3, v126, v96
	v_mfma_f32_16x16x32_bf16 v[84:87], v[68:71], v[32:35], v[76:79]
	ds_read_b128 v[68:71], v125 offset:8896
	v_mul_f32_e32 v3, 0xbfb8aa3b, v3
	v_exp_f32_e32 v3, v3
	s_waitcnt lgkmcnt(0)
	v_mfma_f32_16x16x32_bf16 v[76:79], v[68:71], v[32:35], v[130:133]
	v_add_f32_e32 v3, 1.0, v3
	s_nop 1
	v_rcp_f32_e32 v131, v3
	v_add_f32_e32 v3, v127, v92
	v_add_f32_e32 v92, v126, v97
	v_mul_f32_e32 v92, 0xbfb8aa3b, v92
	v_exp_f32_e32 v92, v92
	v_mul_f32_e32 v3, 0xbfb8aa3b, v3
	v_exp_f32_e32 v3, v3
	v_mfma_f32_16x16x32_bf16 v[80:83], v[68:71], v[16:19], v[134:137]
	v_add_f32_e32 v92, 1.0, v92
	v_rcp_f32_e32 v130, v92
	v_add_f32_e32 v92, v127, v93
	v_mul_f32_e32 v92, 0xbfb8aa3b, v92
	v_exp_f32_e32 v92, v92
	ds_read_b128 v[68:71], v125 offset:13248
	v_add_f32_e32 v3, 1.0, v3
	v_rcp_f32_e32 v3, v3
	v_add_f32_e32 v92, 1.0, v92
	v_rcp_f32_e32 v107, v92
	v_pk_mul_f32 v[92:93], v[130:131], s[96:97] op_sel_hi:[1,0]
	s_waitcnt lgkmcnt(0)
	v_mfma_f32_16x16x32_bf16 v[72:75], v[68:71], v[16:19], v[138:141]
	v_mul_f32_e64 v92, v104, v92
	v_mul_f32_e64 v93, v105, v93
	v_pk_add_f32 v[96:97], v[92:93], v[92:93]
	v_cvt_f16_f32_e32 v93, v93
	v_fmamk_f32 v109, v97, 0x3ab60b61, v226
	v_mul_f32_e32 v130, 0x3fb8aa3b, v97
	v_fmaak_f32 v109, v97, v109, 0x3d2aaaab
	v_exp_f32_e32 v130, v130
	v_fmaak_f32 v109, v97, v109, 0x3e2aaaab
	v_fma_f32 v109, v97, v109, 0.5
	v_fma_f32 v109, v97, v109, 1.0
	v_sub_f32_e32 v130, 1.0, v130
	v_mul_f32_e64 v109, v97, -v109
	v_cmp_lt_f32_e64 s[0:1], s94, v97
	v_cvt_f32_f16_e32 v93, v93
	v_cmp_lt_f32_e32 vcc, s94, v96
	v_cndmask_b32_e64 v97, v130, v109, s[0:1]
	v_sqrt_f32_e32 v97, v97
	ds_read_b32 v109, v113 offset:17408
	v_cvt_f16_f32_e32 v92, v92
	v_mfma_f32_16x16x32_bf16 v[68:71], v[68:71], v[32:35], v[142:145]
	v_mul_f32_e32 v3, v3, v97
	s_waitcnt lgkmcnt(0)
	v_fma_mixlo_f16 v3, v109, v3, 0
	v_cvt_f32_f16_e32 v3, v3
	v_cvt_f32_f16_e32 v92, v92
	v_mov_b32_e32 v109, v1
	ds_write2st64_b32 v113, v3, v93 offset0:68 offset1:196
	v_fmamk_f32 v3, v96, 0x3ab60b61, v226
	v_mul_f32_e32 v93, 0x3fb8aa3b, v96
	v_fmaak_f32 v3, v96, v3, 0x3d2aaaab
	v_exp_f32_e32 v93, v93
	v_fmaak_f32 v3, v96, v3, 0x3e2aaaab
	v_fma_f32 v3, v96, v3, 0.5
	v_fma_f32 v3, v96, v3, 1.0
	v_sub_f32_e32 v93, 1.0, v93
	v_mul_f32_e64 v3, v96, -v3
	s_nop 0
	v_cndmask_b32_e32 v3, v93, v3, vcc
	v_sqrt_f32_e32 v3, v3
	ds_read_b32 v93, v113 offset:17920
	v_mul_f32_e32 v3, v107, v3
	v_ashrrev_i32_e32 v107, 31, v106
	s_waitcnt lgkmcnt(0)
; __device__ __forceinline__ float sigmoidf_(float x) { return __builtin_amdgcn_rcpf(1.0f + __expf(-x)); }
; template <int PASS>
; __device__ __forceinline__ void lru_phase(const Args& a, Frame& F, int l) {
;     ...
;             { const int j = 16 * w + fr; const float bav = bav_u, bxv = bxv_u, sp = sp_u;
; #pragma unroll
;                 for (int m = 0; m < 4; ++m)
; #pragma unroll
;                     for (int r = 0; r < 4; ++r) { const int tt = 16 * m + 4 * fq + r;
;                         const float rr = sigmoidf_(acc[m][0][r] + bav), ii = sigmoidf_(acc[m][1][r] + bxv);
;                         const float la = -8.0f * rr * sp; const float av = __expf(la); const float mult = __builtin_amdgcn_sqrtf(neg_expm1f(2.0f * la));
;                         const float xcv = XC[tt * 128 + j]; (void)av; AA[tt * 128 + j] = (float)(_Float16)la; XC[tt * 128 + j] = (float)(_Float16)(mult * ii * xcv); } }
	v_fma_mixlo_f16 v3, v93, v3, 0
	v_cvt_f32_f16_e32 v3, v3
	ds_write2st64_b32 v113, v3, v92 offset0:70 offset1:198
	v_add_f32_e32 v3, v126, v98
	v_mul_f32_e32 v3, 0xbfb8aa3b, v3
	v_add_f32_e32 v92, v126, v99
	v_exp_f32_e32 v3, v3
	v_mul_f32_e32 v92, 0xbfb8aa3b, v92
	v_exp_f32_e32 v92, v92
	v_add_f32_e32 v3, 1.0, v3
	v_rcp_f32_e32 v93, v3
	v_add_f32_e32 v3, v127, v94
	v_add_f32_e32 v92, 1.0, v92
	v_add_f32_e32 v94, v127, v95
	v_rcp_f32_e32 v92, v92
	v_mul_f32_e32 v94, 0xbfb8aa3b, v94
	v_exp_f32_e32 v94, v94
	v_mul_f32_e32 v3, 0xbfb8aa3b, v3
	v_pk_mul_f32 v[92:93], v[92:93], s[96:97] op_sel_hi:[1,0]
	v_exp_f32_e32 v3, v3
	v_add_f32_e32 v94, 1.0, v94
	v_pk_mul_f32 v[92:93], v[104:105], v[92:93]
	v_rcp_f32_e32 v96, v94
	v_pk_add_f32 v[94:95], v[92:93], v[92:93]
	v_add_f32_e32 v3, 1.0, v3
	v_fmamk_f32 v97, v95, 0x3ab60b61, v226
	v_mul_f32_e32 v98, 0x3fb8aa3b, v95
	v_fmaak_f32 v97, v95, v97, 0x3d2aaaab
	v_exp_f32_e32 v98, v98
	v_fmaak_f32 v97, v95, v97, 0x3e2aaaab
	v_fma_f32 v97, v95, v97, 0.5
	v_fma_f32 v97, v95, v97, 1.0
	v_sub_f32_e32 v98, 1.0, v98
	v_mul_f32_e64 v97, v95, -v97
	v_cmp_lt_f32_e64 s[0:1], s94, v95
	v_rcp_f32_e32 v3, v3
	v_cvt_f16_f32_e32 v93, v93
	v_cndmask_b32_e64 v95, v98, v97, s[0:1]
	v_sqrt_f32_e32 v95, v95
	ds_read_b32 v97, v113 offset:18432
	v_cvt_f32_f16_e32 v93, v93
	v_cmp_lt_f32_e32 vcc, s94, v94
	v_mul_f32_e32 v3, v3, v95
	v_cvt_f16_f32_e32 v92, v92
	s_waitcnt lgkmcnt(0)
	v_fma_mixlo_f16 v3, v97, v3, 0
	v_cvt_f32_f16_e32 v3, v3
	v_cvt_f32_f16_e32 v92, v92
	ds_write2st64_b32 v113, v3, v93 offset0:72 offset1:200
	v_fmamk_f32 v3, v94, 0x3ab60b61, v226
	v_mul_f32_e32 v93, 0x3fb8aa3b, v94
	v_fmaak_f32 v3, v94, v3, 0x3d2aaaab
	v_exp_f32_e32 v93, v93
	v_fmaak_f32 v3, v94, v3, 0x3e2aaaab
	v_fma_f32 v3, v94, v3, 0.5
	v_fma_f32 v3, v94, v3, 1.0
	v_sub_f32_e32 v93, 1.0, v93
	v_mul_f32_e64 v3, v94, -v3
	s_nop 0
	v_cndmask_b32_e32 v3, v93, v3, vcc
	v_sqrt_f32_e32 v3, v3
	ds_read_b32 v93, v113 offset:18944
	v_mul_f32_e32 v3, v96, v3
	s_waitcnt lgkmcnt(0)
	v_fma_mixlo_f16 v3, v93, v3, 0
	v_cvt_f32_f16_e32 v3, v3
	ds_write2st64_b32 v113, v3, v92 offset0:74 offset1:202
	v_add_f32_e32 v3, v126, v88
	v_mul_f32_e32 v3, 0xbfb8aa3b, v3
	v_exp_f32_e32 v3, v3
	s_nop 0
	v_add_f32_e32 v3, 1.0, v3
	v_rcp_f32_e32 v93, v3
	v_add_f32_e32 v3, v127, v84
	v_add_f32_e32 v84, v126, v89
	v_mul_f32_e32 v84, 0xbfb8aa3b, v84
	v_exp_f32_e32 v84, v84
	v_mul_f32_e32 v3, 0xbfb8aa3b, v3
	v_exp_f32_e32 v3, v3
	v_add_f32_e32 v84, 1.0, v84
	v_rcp_f32_e32 v92, v84
	v_add_f32_e32 v84, v127, v85
	v_mul_f32_e32 v84, 0xbfb8aa3b, v84
	v_exp_f32_e32 v84, v84
	v_add_f32_e32 v3, 1.0, v3
	v_rcp_f32_e32 v3, v3
	v_add_f32_e32 v84, 1.0, v84
	v_rcp_f32_e32 v94, v84
	v_pk_mul_f32 v[84:85], v[92:93], s[96:97] op_sel_hi:[1,0]
	s_nop 0
	v_pk_mul_f32 v[84:85], v[104:105], v[84:85]
	s_nop 0
	v_pk_add_f32 v[88:89], v[84:85], v[84:85]
	v_cvt_f16_f32_e32 v85, v85
	v_fmamk_f32 v92, v89, 0x3ab60b61, v226
	v_mul_f32_e32 v93, 0x3fb8aa3b, v89
	v_fmaak_f32 v92, v89, v92, 0x3d2aaaab
	v_exp_f32_e32 v93, v93
	v_fmaak_f32 v92, v89, v92, 0x3e2aaaab
	v_fma_f32 v92, v89, v92, 0.5
	v_fma_f32 v92, v89, v92, 1.0
	v_sub_f32_e32 v93, 1.0, v93
	v_mul_f32_e64 v92, v89, -v92
	v_cmp_lt_f32_e64 s[0:1], s94, v89
	v_cvt_f32_f16_e32 v85, v85
	v_cmp_lt_f32_e32 vcc, s94, v88
	v_cndmask_b32_e64 v89, v93, v92, s[0:1]
	v_sqrt_f32_e32 v89, v89
	ds_read_b32 v92, v113 offset:25600
	v_cvt_f16_f32_e32 v84, v84
	v_mul_f32_e32 v3, v3, v89
	s_waitcnt lgkmcnt(0)
	v_fma_mixlo_f16 v3, v92, v3, 0
	v_cvt_f32_f16_e32 v3, v3
	v_cvt_f32_f16_e32 v84, v84
	ds_write2st64_b32 v113, v3, v85 offset0:100 offset1:228
	v_fmamk_f32 v3, v88, 0x3ab60b61, v226
	v_mul_f32_e32 v85, 0x3fb8aa3b, v88
	v_fmaak_f32 v3, v88, v3, 0x3d2aaaab
	v_exp_f32_e32 v85, v85
	v_fmaak_f32 v3, v88, v3, 0x3e2aaaab
	v_fma_f32 v3, v88, v3, 0.5
	v_fma_f32 v3, v88, v3, 1.0
	v_sub_f32_e32 v85, 1.0, v85
	v_mul_f32_e64 v3, v88, -v3
	s_nop 0
	v_cndmask_b32_e32 v3, v85, v3, vcc
	v_sqrt_f32_e32 v3, v3
	ds_read_b32 v85, v113 offset:26112
	v_mul_f32_e32 v3, v94, v3
	s_waitcnt lgkmcnt(0)
	v_fma_mixlo_f16 v3, v85, v3, 0
	v_cvt_f32_f16_e32 v3, v3
	ds_write2st64_b32 v113, v3, v84 offset0:102 offset1:230
	v_add_f32_e32 v3, v126, v90
	v_mul_f32_e32 v3, 0xbfb8aa3b, v3
	v_add_f32_e32 v84, v126, v91
	v_exp_f32_e32 v3, v3
	v_mul_f32_e32 v84, 0xbfb8aa3b, v84
	v_exp_f32_e32 v84, v84
	v_add_f32_e32 v3, 1.0, v3
	v_rcp_f32_e32 v85, v3
	v_add_f32_e32 v3, v127, v86
	v_add_f32_e32 v84, 1.0, v84
	v_add_f32_e32 v86, v127, v87
	v_rcp_f32_e32 v84, v84
	v_mul_f32_e32 v86, 0xbfb8aa3b, v86
	v_exp_f32_e32 v86, v86
	v_mul_f32_e32 v3, 0xbfb8aa3b, v3
	v_pk_mul_f32 v[84:85], v[84:85], s[96:97] op_sel_hi:[1,0]
	v_exp_f32_e32 v3, v3
	v_add_f32_e32 v86, 1.0, v86
	v_pk_mul_f32 v[84:85], v[104:105], v[84:85]
	v_rcp_f32_e32 v88, v86
	v_pk_add_f32 v[86:87], v[84:85], v[84:85]
	v_add_f32_e32 v3, 1.0, v3
	v_fmamk_f32 v89, v87, 0x3ab60b61, v226
	v_mul_f32_e32 v90, 0x3fb8aa3b, v87
	v_fmaak_f32 v89, v87, v89, 0x3d2aaaab
	v_exp_f32_e32 v90, v90
	v_fmaak_f32 v89, v87, v89, 0x3e2aaaab
	v_fma_f32 v89, v87, v89, 0.5
	v_fma_f32 v89, v87, v89, 1.0
	v_sub_f32_e32 v90, 1.0, v90
	v_mul_f32_e64 v89, v87, -v89
	v_cmp_lt_f32_e64 s[0:1], s94, v87
	v_rcp_f32_e32 v3, v3
	v_cvt_f16_f32_e32 v85, v85
	v_cndmask_b32_e64 v87, v90, v89, s[0:1]
	v_sqrt_f32_e32 v87, v87
	ds_read_b32 v89, v113 offset:26624
	v_cvt_f32_f16_e32 v85, v85
	v_cmp_lt_f32_e32 vcc, s94, v86
	v_mul_f32_e32 v3, v3, v87
	v_cvt_f16_f32_e32 v84, v84
	s_waitcnt lgkmcnt(0)
; __device__ __forceinline__ float sigmoidf_(float x) { return __builtin_amdgcn_rcpf(1.0f + __expf(-x)); }
; template <int PASS>
; __device__ __forceinline__ void lru_phase(const Args& a, Frame& F, int l) {
;     ...
;             { const int j = 16 * w + fr; const float bav = bav_u, bxv = bxv_u, sp = sp_u;
; #pragma unroll
;                 for (int m = 0; m < 4; ++m)
; #pragma unroll
;                     for (int r = 0; r < 4; ++r) { const int tt = 16 * m + 4 * fq + r;
;                         const float rr = sigmoidf_(acc[m][0][r] + bav), ii = sigmoidf_(acc[m][1][r] + bxv);
;                         const float la = -8.0f * rr * sp; const float av = __expf(la); const float mult = __builtin_amdgcn_sqrtf(neg_expm1f(2.0f * la));
;                         const float xcv = XC[tt * 128 + j]; (void)av; AA[tt * 128 + j] = (float)(_Float16)la; XC[tt * 128 + j] = (float)(_Float16)(mult * ii * xcv); } }
	v_fma_mixlo_f16 v3, v89, v3, 0
	v_cvt_f32_f16_e32 v3, v3
	v_cvt_f32_f16_e32 v84, v84
	ds_write2st64_b32 v113, v3, v85 offset0:104 offset1:232
	v_fmamk_f32 v3, v86, 0x3ab60b61, v226
	v_mul_f32_e32 v85, 0x3fb8aa3b, v86
	v_fmaak_f32 v3, v86, v3, 0x3d2aaaab
	v_exp_f32_e32 v85, v85
	v_fmaak_f32 v3, v86, v3, 0x3e2aaaab
	v_fma_f32 v3, v86, v3, 0.5
	v_fma_f32 v3, v86, v3, 1.0
	v_sub_f32_e32 v85, 1.0, v85
	v_mul_f32_e64 v3, v86, -v3
	s_nop 0
	v_cndmask_b32_e32 v3, v85, v3, vcc
	v_sqrt_f32_e32 v3, v3
	ds_read_b32 v85, v113 offset:27136
	v_mul_f32_e32 v3, v88, v3
	s_waitcnt lgkmcnt(0)
	v_fma_mixlo_f16 v3, v85, v3, 0
	v_cvt_f32_f16_e32 v3, v3
	ds_write2st64_b32 v113, v3, v84 offset0:106 offset1:234
	v_add_f32_e32 v3, v126, v80
	v_mul_f32_e32 v3, 0xbfb8aa3b, v3
	v_exp_f32_e32 v3, v3
	s_nop 0
	v_add_f32_e32 v3, 1.0, v3
	v_rcp_f32_e32 v85, v3
	v_add_f32_e32 v3, v127, v76
	v_add_f32_e32 v76, v126, v81
	v_mul_f32_e32 v76, 0xbfb8aa3b, v76
	v_exp_f32_e32 v76, v76
	v_mul_f32_e32 v3, 0xbfb8aa3b, v3
	v_exp_f32_e32 v3, v3
	v_add_f32_e32 v76, 1.0, v76
	v_rcp_f32_e32 v84, v76
	v_add_f32_e32 v76, v127, v77
	v_mul_f32_e32 v76, 0xbfb8aa3b, v76
	v_exp_f32_e32 v76, v76
	v_add_f32_e32 v3, 1.0, v3
	v_rcp_f32_e32 v3, v3
	v_add_f32_e32 v76, 1.0, v76
	v_rcp_f32_e32 v86, v76
	v_pk_mul_f32 v[76:77], v[84:85], s[96:97] op_sel_hi:[1,0]
	s_nop 0
	v_pk_mul_f32 v[76:77], v[104:105], v[76:77]
	s_nop 0
	v_pk_add_f32 v[80:81], v[76:77], v[76:77]
	v_cvt_f16_f32_e32 v77, v77
	v_fmamk_f32 v84, v81, 0x3ab60b61, v226
	v_mul_f32_e32 v85, 0x3fb8aa3b, v81
	v_fmaak_f32 v84, v81, v84, 0x3d2aaaab
	v_exp_f32_e32 v85, v85
	v_fmaak_f32 v84, v81, v84, 0x3e2aaaab
	v_fma_f32 v84, v81, v84, 0.5
	v_fma_f32 v84, v81, v84, 1.0
	v_sub_f32_e32 v85, 1.0, v85
	v_mul_f32_e64 v84, v81, -v84
	v_cmp_lt_f32_e64 s[0:1], s94, v81
	v_cvt_f32_f16_e32 v77, v77
	v_cmp_lt_f32_e32 vcc, s94, v80
	v_cndmask_b32_e64 v81, v85, v84, s[0:1]
	v_sqrt_f32_e32 v81, v81
	ds_read_b32 v84, v113 offset:33792
	ds_write_b32 v114, v77
	v_mul_f32_e32 v77, 0x3fb8aa3b, v80
	v_mul_f32_e32 v3, v3, v81
	v_exp_f32_e32 v77, v77
	s_waitcnt lgkmcnt(1)
	v_fma_mixlo_f16 v3, v84, v3, 0
	v_cvt_f32_f16_e32 v3, v3
	v_cvt_f16_f32_e32 v76, v76
	v_sub_f32_e32 v77, 1.0, v77
	ds_write_b32 v113, v3 offset:33792
	v_fmamk_f32 v3, v80, 0x3ab60b61, v226
	v_fmaak_f32 v3, v80, v3, 0x3d2aaaab
	v_fmaak_f32 v3, v80, v3, 0x3e2aaaab
	v_fma_f32 v3, v80, v3, 0.5
	v_fma_f32 v3, v80, v3, 1.0
	v_mul_f32_e64 v3, v80, -v3
	v_cvt_f32_f16_e32 v76, v76
	v_cndmask_b32_e32 v3, v77, v3, vcc
	v_sqrt_f32_e32 v3, v3
	ds_read_b32 v77, v113 offset:34304
	ds_write_b32 v115, v76
	v_add_f32_e32 v76, v126, v83
	v_mul_f32_e32 v3, v86, v3
	v_mul_f32_e32 v76, 0xbfb8aa3b, v76
	s_waitcnt lgkmcnt(1)
	v_fma_mixlo_f16 v3, v77, v3, 0
	v_cvt_f32_f16_e32 v3, v3
	v_exp_f32_e32 v76, v76
	ds_write_b32 v113, v3 offset:34304
	v_add_f32_e32 v3, v126, v82
	v_mul_f32_e32 v3, 0xbfb8aa3b, v3
	v_exp_f32_e32 v3, v3
	v_add_f32_e32 v76, 1.0, v76
	v_rcp_f32_e32 v76, v76
	v_add_f32_e32 v3, 1.0, v3
	v_rcp_f32_e32 v77, v3
	v_add_f32_e32 v3, v127, v78
	v_add_f32_e32 v78, v127, v79
	v_mul_f32_e32 v78, 0xbfb8aa3b, v78
	v_exp_f32_e32 v78, v78
	v_pk_mul_f32 v[76:77], v[76:77], s[96:97] op_sel_hi:[1,0]
	v_mul_f32_e32 v3, 0xbfb8aa3b, v3
	v_pk_mul_f32 v[76:77], v[104:105], v[76:77]
	v_add_f32_e32 v78, 1.0, v78
	v_rcp_f32_e32 v80, v78
	v_pk_add_f32 v[78:79], v[76:77], v[76:77]
	v_exp_f32_e32 v3, v3
	v_fmamk_f32 v81, v79, 0x3ab60b61, v226
	v_mul_f32_e32 v82, 0x3fb8aa3b, v79
	v_fmaak_f32 v81, v79, v81, 0x3d2aaaab
	v_exp_f32_e32 v82, v82
	v_fmaak_f32 v81, v79, v81, 0x3e2aaaab
	v_fma_f32 v81, v79, v81, 0.5
	v_fma_f32 v81, v79, v81, 1.0
	v_sub_f32_e32 v82, 1.0, v82
	v_mul_f32_e64 v81, v79, -v81
	v_cmp_lt_f32_e64 s[0:1], s94, v79
	v_add_f32_e32 v3, 1.0, v3
	v_rcp_f32_e32 v3, v3
	v_cndmask_b32_e64 v79, v82, v81, s[0:1]
	v_sqrt_f32_e32 v79, v79
	ds_read_b32 v81, v113 offset:34816
	v_cvt_f16_f32_e32 v77, v77
	v_cmp_lt_f32_e32 vcc, s94, v78
	v_mul_f32_e32 v3, v3, v79
	v_cvt_f16_f32_e32 v76, v76
	s_waitcnt lgkmcnt(0)
	v_fma_mixlo_f16 v3, v81, v3, 0
	v_cvt_f32_f16_e32 v77, v77
	v_cvt_f32_f16_e32 v3, v3
	v_cvt_f32_f16_e32 v76, v76
	ds_write_b32 v116, v77
	ds_write_b32 v113, v3 offset:34816
	v_fmamk_f32 v3, v78, 0x3ab60b61, v226
	v_mul_f32_e32 v77, 0x3fb8aa3b, v78
	v_fmaak_f32 v3, v78, v3, 0x3d2aaaab
	v_exp_f32_e32 v77, v77
	v_fmaak_f32 v3, v78, v3, 0x3e2aaaab
	v_fma_f32 v3, v78, v3, 0.5
	v_fma_f32 v3, v78, v3, 1.0
	v_sub_f32_e32 v77, 1.0, v77
	v_mul_f32_e64 v3, v78, -v3
	s_nop 0
	v_cndmask_b32_e32 v3, v77, v3, vcc
	v_sqrt_f32_e32 v3, v3
	ds_read_b32 v77, v113 offset:35328
	ds_write_b32 v117, v76
	v_mul_f32_e32 v3, v80, v3
	s_waitcnt lgkmcnt(1)
	v_fma_mixlo_f16 v3, v77, v3, 0
	v_cvt_f32_f16_e32 v3, v3
	ds_write_b32 v113, v3 offset:35328
	v_add_f32_e32 v3, v126, v72
	v_mul_f32_e32 v3, 0xbfb8aa3b, v3
	v_exp_f32_e32 v3, v3
	s_nop 0
	v_add_f32_e32 v3, 1.0, v3
	v_rcp_f32_e32 v77, v3
	v_add_f32_e32 v3, v127, v68
	v_add_f32_e32 v68, v126, v73
	v_mul_f32_e32 v68, 0xbfb8aa3b, v68
	v_exp_f32_e32 v68, v68
	v_mul_f32_e32 v3, 0xbfb8aa3b, v3
	v_exp_f32_e32 v3, v3
	v_add_f32_e32 v68, 1.0, v68
	v_rcp_f32_e32 v76, v68
	v_add_f32_e32 v68, v127, v69
	v_mul_f32_e32 v68, 0xbfb8aa3b, v68
	v_exp_f32_e32 v68, v68
	v_add_f32_e32 v3, 1.0, v3
	v_rcp_f32_e32 v3, v3
	v_add_f32_e32 v68, 1.0, v68
	v_rcp_f32_e32 v78, v68
	v_pk_mul_f32 v[68:69], v[76:77], s[96:97] op_sel_hi:[1,0]
	s_nop 0
	v_pk_mul_f32 v[68:69], v[104:105], v[68:69]
	s_nop 0
	v_pk_add_f32 v[72:73], v[68:69], v[68:69]
	v_cvt_f16_f32_e32 v69, v69
	v_fmamk_f32 v76, v73, 0x3ab60b61, v226
	v_mul_f32_e32 v77, 0x3fb8aa3b, v73
	v_fmaak_f32 v76, v73, v76, 0x3d2aaaab
	v_exp_f32_e32 v77, v77
	v_fmaak_f32 v76, v73, v76, 0x3e2aaaab
	v_fma_f32 v76, v73, v76, 0.5
	v_fma_f32 v76, v73, v76, 1.0
	v_sub_f32_e32 v77, 1.0, v77
	v_mul_f32_e64 v76, v73, -v76
	v_cmp_lt_f32_e64 s[0:1], s94, v73
	v_cvt_f32_f16_e32 v69, v69
	v_cmp_lt_f32_e32 vcc, s94, v72
	v_cndmask_b32_e64 v73, v77, v76, s[0:1]
	v_sqrt_f32_e32 v73, v73
	ds_read_b32 v76, v113 offset:41984
	ds_write_b32 v118, v69
	v_mul_f32_e32 v69, 0x3fb8aa3b, v72
	v_mul_f32_e32 v3, v3, v73
	v_exp_f32_e32 v69, v69
	s_waitcnt lgkmcnt(1)
; __device__ __forceinline__ float sigmoidf_(float x) { return __builtin_amdgcn_rcpf(1.0f + __expf(-x)); }
; template <int PASS>
; __device__ __forceinline__ void lru_phase(const Args& a, Frame& F, int l) {
;     ...
;             { const int j = 16 * w + fr; const float bav = bav_u, bxv = bxv_u, sp = sp_u;
; #pragma unroll
;                 for (int m = 0; m < 4; ++m)
; #pragma unroll
;                     for (int r = 0; r < 4; ++r) { const int tt = 16 * m + 4 * fq + r;
;                         const float rr = sigmoidf_(acc[m][0][r] + bav), ii = sigmoidf_(acc[m][1][r] + bxv);
;                         const float la = -8.0f * rr * sp; const float av = __expf(la); const float mult = __builtin_amdgcn_sqrtf(neg_expm1f(2.0f * la));
;                         const float xcv = XC[tt * 128 + j]; (void)av; AA[tt * 128 + j] = (float)(_Float16)la; XC[tt * 128 + j] = (float)(_Float16)(mult * ii * xcv); } }
;             __syncthreads();
;             if (PASS == 1) { const int row = tl >> 3, seg = tl & 7; unsigned short* LAg = (unsigned short*)(F.ws + WS_LA) + ((size_t)b * SEQ + t0 + row) * BW + h * 128 + seg * 16; unsigned short* LBg = (unsigned short*)(F.ws + WS_LB) + ((size_t)b * SEQ + t0 + row) * BW + h * 128 + seg * 16;
	v_fma_mixlo_f16 v3, v76, v3, 0
	v_cvt_f32_f16_e32 v3, v3
	v_cvt_f16_f32_e32 v68, v68
	v_sub_f32_e32 v69, 1.0, v69
	ds_write_b32 v113, v3 offset:41984
	v_fmamk_f32 v3, v72, 0x3ab60b61, v226
	v_fmaak_f32 v3, v72, v3, 0x3d2aaaab
	v_fmaak_f32 v3, v72, v3, 0x3e2aaaab
	v_fma_f32 v3, v72, v3, 0.5
	v_fma_f32 v3, v72, v3, 1.0
	v_mul_f32_e64 v3, v72, -v3
	v_cvt_f32_f16_e32 v68, v68
	v_cndmask_b32_e32 v3, v69, v3, vcc
	v_sqrt_f32_e32 v3, v3
	ds_read_b32 v69, v113 offset:42496
	ds_write_b32 v119, v68
	v_add_f32_e32 v68, v126, v75
	v_mul_f32_e32 v3, v78, v3
	v_mul_f32_e32 v68, 0xbfb8aa3b, v68
	s_waitcnt lgkmcnt(1)
	v_fma_mixlo_f16 v3, v69, v3, 0
	v_cvt_f32_f16_e32 v3, v3
	v_exp_f32_e32 v68, v68
	ds_write_b32 v113, v3 offset:42496
	v_add_f32_e32 v3, v126, v74
	v_mul_f32_e32 v3, 0xbfb8aa3b, v3
	v_exp_f32_e32 v3, v3
	v_add_f32_e32 v68, 1.0, v68
	v_rcp_f32_e32 v68, v68
	v_add_f32_e32 v3, 1.0, v3
	v_rcp_f32_e32 v69, v3
	v_add_f32_e32 v3, v127, v70
	v_add_f32_e32 v70, v127, v71
	v_mul_f32_e32 v70, 0xbfb8aa3b, v70
	v_exp_f32_e32 v70, v70
	v_pk_mul_f32 v[68:69], v[68:69], s[96:97] op_sel_hi:[1,0]
	v_mul_f32_e32 v3, 0xbfb8aa3b, v3
	v_pk_mul_f32 v[68:69], v[104:105], v[68:69]
	v_add_f32_e32 v70, 1.0, v70
	v_rcp_f32_e32 v72, v70
	v_pk_add_f32 v[70:71], v[68:69], v[68:69]
	v_exp_f32_e32 v3, v3
	v_fmamk_f32 v73, v71, 0x3ab60b61, v226
	v_mul_f32_e32 v74, 0x3fb8aa3b, v71
	v_fmaak_f32 v73, v71, v73, 0x3d2aaaab
	v_exp_f32_e32 v74, v74
	v_fmaak_f32 v73, v71, v73, 0x3e2aaaab
	v_fma_f32 v73, v71, v73, 0.5
	v_fma_f32 v73, v71, v73, 1.0
	v_sub_f32_e32 v74, 1.0, v74
	v_mul_f32_e64 v73, v71, -v73
	v_cmp_lt_f32_e64 s[0:1], s94, v71
	v_add_f32_e32 v3, 1.0, v3
	v_rcp_f32_e32 v3, v3
	v_cndmask_b32_e64 v71, v74, v73, s[0:1]
	v_sqrt_f32_e32 v71, v71
	ds_read_b32 v73, v113 offset:43008
	v_cvt_f16_f32_e32 v69, v69
	v_cmp_lt_f32_e32 vcc, s94, v70
	v_mul_f32_e32 v3, v3, v71
	v_cvt_f16_f32_e32 v68, v68
	s_waitcnt lgkmcnt(0)
	v_fma_mixlo_f16 v3, v73, v3, 0
	v_cvt_f32_f16_e32 v69, v69
	v_cvt_f32_f16_e32 v3, v3
	v_cvt_f32_f16_e32 v68, v68
	s_add_u32 s0, s60, s3
	ds_write_b32 v120, v69
	ds_write_b32 v113, v3 offset:43008
	v_fmamk_f32 v3, v70, 0x3ab60b61, v226
	v_mul_f32_e32 v69, 0x3fb8aa3b, v70
	v_fmaak_f32 v3, v70, v3, 0x3d2aaaab
	v_exp_f32_e32 v69, v69
	v_fmaak_f32 v3, v70, v3, 0x3e2aaaab
	v_fma_f32 v3, v70, v3, 0.5
	v_fma_f32 v3, v70, v3, 1.0
	v_sub_f32_e32 v69, 1.0, v69
	v_mul_f32_e64 v3, v70, -v3
	s_addc_u32 s1, s61, 0
	v_cndmask_b32_e32 v3, v69, v3, vcc
	v_sqrt_f32_e32 v3, v3
	ds_read_b32 v69, v113 offset:43520
	ds_write_b32 v121, v68
	v_cmp_lt_i32_e32 vcc, 0, v2
	v_mul_f32_e32 v3, v72, v3
	s_waitcnt lgkmcnt(1)
	v_fma_mixlo_f16 v3, v69, v3, 0
	v_cvt_f32_f16_e32 v3, v3
	v_lshl_add_u64 v[68:69], s[0:1], 0, v[106:107]
	v_lshlrev_b64 v[68:69], 11, v[68:69]
	v_lshl_add_u64 v[70:71], s[62:63], 0, v[68:69]
	ds_write_b32 v113, v3 offset:43520
	v_lshlrev_b32_e32 v3, 2, v129
	v_lshl_or_b32 v3, v106, 9, v3
	v_lshl_add_u64 v[68:69], s[64:65], 0, v[68:69]
	v_add_u32_e32 v3, 0, v3
	s_waitcnt lgkmcnt(0)
	s_barrier
; #define GAS __attribute__((address_space(1)))
; __device__ __forceinline__ u32x4 pack8h(const float (&o)[8]) { u32x4 w; w.x = pkh2(o[0], o[1]); w.y = pkh2(o[2], o[3]); w.z = pkh2(o[4], o[5]); w.w = pkh2(o[6], o[7]); return w; }
; template <int PASS>
; __device__ __forceinline__ void lru_phase(const Args& a, Frame& F, int l) {
;     ...
;             if (PASS == 1) { const int row = tl >> 3, seg = tl & 7; unsigned short* LAg = (unsigned short*)(F.ws + WS_LA) + ((size_t)b * SEQ + t0 + row) * BW + h * 128 + seg * 16; unsigned short* LBg = (unsigned short*)(F.ws + WS_LB) + ((size_t)b * SEQ + t0 + row) * BW + h * 128 + seg * 16;
; #pragma unroll
;                 for (int j = 0; j < 2; ++j) { float va[8], vb[8];
; #pragma unroll
;                     for (int e = 0; e < 8; ++e) { va[e] = AA[row * 128 + seg * 16 + 8 * j + e]; vb[e] = XC[row * 128 + seg * 16 + 8 * j + e]; }
;                     *(GAS u32x4*)(LAg + 8 * j) = pack8h(va); *(GAS u32x4*)(LBg + 8 * j) = pack8h(vb); } }
;             { float qa = 1.f, qb = 0.f;
; #pragma unroll
;                 for (int tt = 16 * qd; tt < 16 * qd + 16; ++tt) { const float av = __expf(AA[tt * 128 + jch]); qb = av * qb + XC[tt * 128 + jch]; qa *= av; }
;                 QA[qd * 128 + jch] = qa; QB[qd * 128 + jch] = qb; }
	v_lshl_add_u64 v[92:93], v[70:71], 0, v[108:109]
	v_lshl_add_u64 v[94:95], v[68:69], 0, v[108:109]
	ds_read_b128 v[68:71], v3 offset:50176
	ds_read_b128 v[72:75], v3 offset:17408
	ds_read_b128 v[76:79], v3 offset:17424
	ds_read_b128 v[80:83], v3 offset:17440
	ds_read_b128 v[84:87], v3 offset:17456
	ds_read_b128 v[88:91], v3 offset:50192
	s_waitcnt lgkmcnt(5)
	v_cvt_pk_f16_f32 v68, v68, v69
	v_cvt_pk_f16_f32 v69, v70, v71
	s_lshl_b32 s0, s2, 7
	s_and_b32 s0, s0, 0x80
	s_waitcnt lgkmcnt(0)
	v_cvt_pk_f16_f32 v70, v88, v89
	v_cvt_pk_f16_f32 v71, v90, v91
	global_store_dwordx4 v[92:93], v[68:71], off
	s_nop 1
	v_cvt_pk_f16_f32 v68, v72, v73
	v_cvt_pk_f16_f32 v69, v74, v75
	v_cvt_pk_f16_f32 v70, v76, v77
	v_cvt_pk_f16_f32 v71, v78, v79
	global_store_dwordx4 v[94:95], v[68:71], off
	ds_read_b128 v[68:71], v3 offset:50208
	ds_read_b128 v[72:75], v3 offset:50224
	v_lshlrev_b32_e32 v3, 2, v0
	v_lshl_or_b32 v3, v2, 13, v3
	v_add_u32_e32 v3, 0, v3
	s_waitcnt lgkmcnt(1)
	v_cvt_pk_f16_f32 v68, v68, v69
	v_cvt_pk_f16_f32 v69, v70, v71
	s_waitcnt lgkmcnt(0)
	v_cvt_pk_f16_f32 v70, v72, v73
	v_cvt_pk_f16_f32 v71, v74, v75
	global_store_dwordx4 v[92:93], v[68:71], off offset:16
	ds_read2st64_b32 v[72:73], v3 offset0:72 offset1:74
	ds_read2st64_b32 v[192:193], v3 offset0:196 offset1:198
	ds_read2st64_b32 v[200:201], v3 offset0:68 offset1:70
	ds_read2st64_b32 v[202:203], v3 offset0:200 offset1:202
	ds_read2st64_b32 v[204:205], v3 offset0:204 offset1:206
	ds_read2st64_b32 v[206:207], v3 offset0:76 offset1:78
	ds_read2st64_b32 v[208:209], v3 offset0:208 offset1:210
	ds_read2st64_b32 v[210:211], v3 offset0:80 offset1:82
	ds_read2st64_b32 v[212:213], v3 offset0:212 offset1:214
	ds_read2st64_b32 v[214:215], v3 offset0:84 offset1:86
	ds_read2st64_b32 v[216:217], v3 offset0:216 offset1:218
	ds_read2st64_b32 v[218:219], v3 offset0:88 offset1:90
	ds_read2st64_b32 v[220:221], v3 offset0:220 offset1:222
	ds_read2st64_b32 v[236:237], v3 offset0:92 offset1:94
	ds_read2st64_b32 v[238:239], v3 offset0:224 offset1:226
	s_waitcnt lgkmcnt(14)
	ds_read2st64_b32 v[240:241], v3 offset0:96 offset1:98
	s_nop 0
	v_cvt_pk_f16_f32 v68, v80, v81
	v_cvt_pk_f16_f32 v69, v82, v83
	v_cvt_pk_f16_f32 v70, v84, v85
	v_cvt_pk_f16_f32 v71, v86, v87
	global_store_dwordx4 v[94:95], v[68:71], off offset:16
	s_nop 1
	s_waitcnt lgkmcnt(14)
	v_mov_b32_e32 v68, v192
	v_mov_b32_e32 v69, v193
	s_waitcnt lgkmcnt(13)
	v_mov_b32_e32 v70, v200
	v_mov_b32_e32 v71, v201
	s_waitcnt lgkmcnt(1)
	v_mul_f32_e32 v68, 0x3fb8aa3b, v68
	v_exp_f32_e32 v68, v68
	v_mul_f32_e32 v69, 0x3fb8aa3b, v69
	v_exp_f32_e32 v69, v69
	s_waitcnt lgkmcnt(0)
	v_fma_f32 v70, 0, v68, v70
	v_fmac_f32_e32 v71, v70, v69
	v_mul_f32_e32 v70, v68, v69
	s_waitcnt lgkmcnt(12)
	v_mov_b32_e32 v68, v202
	v_mov_b32_e32 v69, v203
	s_waitcnt lgkmcnt(0)
	v_mul_f32_e32 v68, 0x3fb8aa3b, v68
	v_exp_f32_e32 v68, v68
	v_mul_f32_e32 v69, 0x3fb8aa3b, v69
	v_exp_f32_e32 v69, v69
	v_fma_f32 v71, v71, v68, v72
	v_mul_f32_e32 v68, v70, v68
	v_fmac_f32_e32 v73, v71, v69
	v_mul_f32_e32 v72, v68, v69
	s_waitcnt lgkmcnt(11)
	v_mov_b32_e32 v68, v204
	v_mov_b32_e32 v69, v205
	s_waitcnt lgkmcnt(10)
	v_mov_b32_e32 v70, v206
	v_mov_b32_e32 v71, v207
	s_waitcnt lgkmcnt(1)
	v_mul_f32_e32 v68, 0x3fb8aa3b, v68
	v_exp_f32_e32 v68, v68
	v_mul_f32_e32 v69, 0x3fb8aa3b, v69
	v_exp_f32_e32 v69, v69
	s_waitcnt lgkmcnt(0)
	v_fma_f32 v70, v73, v68, v70
	v_mul_f32_e32 v68, v72, v68
	v_fmac_f32_e32 v71, v70, v69
	v_mul_f32_e32 v70, v68, v69
	s_waitcnt lgkmcnt(9)
	v_mov_b32_e32 v68, v208
	v_mov_b32_e32 v69, v209
	s_waitcnt lgkmcnt(8)
	v_mov_b32_e32 v72, v210
	v_mov_b32_e32 v73, v211
	s_waitcnt lgkmcnt(1)
	v_mul_f32_e32 v68, 0x3fb8aa3b, v68
	v_exp_f32_e32 v68, v68
	v_mul_f32_e32 v69, 0x3fb8aa3b, v69
	v_exp_f32_e32 v69, v69
	s_waitcnt lgkmcnt(0)
	v_fma_f32 v71, v71, v68, v72
	v_mul_f32_e32 v68, v70, v68
	v_fmac_f32_e32 v73, v71, v69
	v_mul_f32_e32 v72, v68, v69
	s_waitcnt lgkmcnt(7)
	v_mov_b32_e32 v68, v212
	v_mov_b32_e32 v69, v213
	s_waitcnt lgkmcnt(6)
	v_mov_b32_e32 v70, v214
	v_mov_b32_e32 v71, v215
	s_waitcnt lgkmcnt(1)
	v_mul_f32_e32 v68, 0x3fb8aa3b, v68
	v_exp_f32_e32 v68, v68
	v_mul_f32_e32 v69, 0x3fb8aa3b, v69
	v_exp_f32_e32 v69, v69
	s_waitcnt lgkmcnt(0)
	v_fma_f32 v70, v73, v68, v70
	v_mul_f32_e32 v68, v72, v68
	v_fmac_f32_e32 v71, v70, v69
	v_mul_f32_e32 v70, v68, v69
	s_waitcnt lgkmcnt(5)
	v_mov_b32_e32 v68, v216
	v_mov_b32_e32 v69, v217
	s_waitcnt lgkmcnt(4)
	v_mov_b32_e32 v72, v218
	v_mov_b32_e32 v73, v219
	s_waitcnt lgkmcnt(1)
	v_mul_f32_e32 v68, 0x3fb8aa3b, v68
	v_exp_f32_e32 v68, v68
	v_mul_f32_e32 v69, 0x3fb8aa3b, v69
	v_exp_f32_e32 v69, v69
	s_waitcnt lgkmcnt(0)
	v_fma_f32 v71, v71, v68, v72
	v_mul_f32_e32 v68, v70, v68
	v_fmac_f32_e32 v73, v71, v69
	v_mul_f32_e32 v72, v68, v69
	s_waitcnt lgkmcnt(3)
	v_mov_b32_e32 v68, v220
	v_mov_b32_e32 v69, v221
	s_waitcnt lgkmcnt(2)
	v_mov_b32_e32 v70, v236
	v_mov_b32_e32 v71, v237
	s_waitcnt lgkmcnt(1)
	v_mul_f32_e32 v68, 0x3fb8aa3b, v68
	v_exp_f32_e32 v68, v68
	v_mul_f32_e32 v69, 0x3fb8aa3b, v69
	v_exp_f32_e32 v69, v69
	s_waitcnt lgkmcnt(0)
	v_fma_f32 v70, v73, v68, v70
	v_mul_f32_e32 v68, v72, v68
	v_fmac_f32_e32 v71, v70, v69
	v_mul_f32_e32 v70, v68, v69
	s_waitcnt lgkmcnt(1)
	v_mov_b32_e32 v68, v238
	v_mov_b32_e32 v69, v239
	s_waitcnt lgkmcnt(0)
	v_mov_b32_e32 v72, v240
	v_mov_b32_e32 v73, v241
	s_waitcnt lgkmcnt(1)
	v_mul_f32_e32 v68, 0x3fb8aa3b, v68
	v_exp_f32_e32 v68, v68
	v_mul_f32_e32 v69, 0x3fb8aa3b, v69
	v_exp_f32_e32 v69, v69
	s_waitcnt lgkmcnt(0)
	v_fma_f32 v3, v71, v68, v72
	v_mul_f32_e32 v68, v70, v68
	v_fmac_f32_e32 v73, v3, v69
	v_mul_f32_e32 v68, v68, v69
	v_lshl_add_u32 v69, v128, 2, 0
	v_add_u32_e32 v3, 0x1c400, v69
	ds_write_b32 v3, v68
	v_or_b32_e32 v68, s0, v0
	v_lshl_add_u32 v70, v68, 2, 0
	v_add_u32_e32 v69, 0x1cc00, v69
	v_add_u32_e32 v70, 0x1d400, v70
	ds_write_b32 v69, v73
	s_waitcnt lgkmcnt(0)
	s_barrier
	ds_read_b32 v70, v70
	s_and_saveexec_b64 s[0:1], vcc
	s_cbranch_execz .LBB0_361
	s_add_i32 s2, 0, 0x1cc00
	v_lshl_add_u32 v71, v0, 2, s2
	s_mov_b64 s[2:3], 0
	v_mov_b32_e32 v72, v2
